# v38 + s_setprio 1 for compute waves 4-7 during the mask scan
# baseline (speedup 1.0000x reference)
_Z7k_gemm1PKfS0_PKDv4_jPKiPiS6_P15HIP_vector_typeIiLj2EEPDF16_S0_S6_S9_:
	v_lshrrev_b32_e32 v142, 6, v0
	s_mov_b32 s10, s2
	v_readfirstlane_b32 s90, v0
	s_nop 0
	s_cmp_lt_u32 s90, 0x100
	s_cbranch_scc1 .Lg1_prio_done
	s_cmp_ge_u32 s90, 0x200
	s_cbranch_scc1 .Lg1_prio_done
	s_setprio 1
.Lg1_prio_done:
	s_load_dwordx4 s[24:27], s[0:1], 0x40
	s_load_dwordx8 s[12:19], s[0:1], 0x0
	s_load_dwordx4 s[20:23], s[0:1], 0x20
	s_load_dwordx2 s[28:29], s[0:1], 0x30
	v_and_b32_e32 v160, 31, v0
	v_bfe_u32 v1, v0, 5, 1
	v_lshlrev_b32_e32 v161, 5, v142
	s_movk_i32 s2, 0xe0
	v_and_or_b32 v2, v161, s2, v160
	v_lshlrev_b32_e32 v3, 4, v1
	v_lshl_or_b32 v2, v2, 5, v3
	v_mov_b32_e32 v3, 0
	s_movk_i32 s2, 0x200
	v_and_b32_e32 v4, 63, v0
	s_waitcnt lgkmcnt(0)
	v_lshl_add_u64 v[158:159], s[16:17], 0, v[2:3]
	v_cmp_gt_u32_e32 vcc, s2, v0
	s_and_saveexec_b64 s[2:3], vcc
	s_cbranch_execz .LBB1_2
	v_add_co_u32_e32 v6, vcc, 0x2000, v158
	s_nop 1
	v_addc_co_u32_e32 v7, vcc, 0, v159, vcc
	global_load_dwordx4 v[18:21], v[158:159], off
	global_load_dwordx4 v[90:93], v[6:7], off
	v_add_co_u32_e32 v6, vcc, 0x4000, v158
	s_nop 1
	v_addc_co_u32_e32 v7, vcc, 0, v159, vcc
	v_add_co_u32_e32 v8, vcc, 0x6000, v158
	s_nop 1
	v_addc_co_u32_e32 v9, vcc, 0, v159, vcc
	global_load_dwordx4 v[86:89], v[6:7], off
	global_load_dwordx4 v[82:85], v[8:9], off
	v_add_co_u32_e32 v6, vcc, 0x8000, v158
	s_nop 1
	v_addc_co_u32_e32 v7, vcc, 0, v159, vcc
	v_add_co_u32_e32 v8, vcc, 0xa000, v158
	s_nop 1
	v_addc_co_u32_e32 v9, vcc, 0, v159, vcc
	global_load_dwordx4 v[78:81], v[6:7], off
	global_load_dwordx4 v[74:77], v[8:9], off
	v_add_co_u32_e32 v6, vcc, 0xc000, v158
	s_nop 1
	v_addc_co_u32_e32 v7, vcc, 0, v159, vcc
	v_add_co_u32_e32 v8, vcc, 0xe000, v158
	s_nop 1
	v_addc_co_u32_e32 v9, vcc, 0, v159, vcc
	global_load_dwordx4 v[70:73], v[6:7], off
	global_load_dwordx4 v[66:69], v[8:9], off
	v_add_co_u32_e32 v6, vcc, 0x10000, v158
	s_nop 1
	v_addc_co_u32_e32 v7, vcc, 0, v159, vcc
	v_add_co_u32_e32 v8, vcc, 0x12000, v158
	s_nop 1
	v_addc_co_u32_e32 v9, vcc, 0, v159, vcc
	global_load_dwordx4 v[62:65], v[6:7], off
	global_load_dwordx4 v[58:61], v[8:9], off
	v_add_co_u32_e32 v6, vcc, 0x14000, v158
	s_nop 1
	v_addc_co_u32_e32 v7, vcc, 0, v159, vcc
	v_add_co_u32_e32 v8, vcc, 0x16000, v158
	s_nop 1
	v_addc_co_u32_e32 v9, vcc, 0, v159, vcc
	global_load_dwordx4 v[54:57], v[6:7], off
	global_load_dwordx4 v[50:53], v[8:9], off
	v_add_co_u32_e32 v6, vcc, 0x18000, v158
	s_nop 1
	v_addc_co_u32_e32 v7, vcc, 0, v159, vcc
	v_add_co_u32_e32 v8, vcc, 0x1a000, v158
	s_nop 1
	v_addc_co_u32_e32 v9, vcc, 0, v159, vcc
	global_load_dwordx4 v[46:49], v[6:7], off
	global_load_dwordx4 v[42:45], v[8:9], off
	v_add_co_u32_e32 v6, vcc, 0x1c000, v158
	s_nop 1
	v_addc_co_u32_e32 v7, vcc, 0, v159, vcc
	v_add_co_u32_e32 v8, vcc, 0x1e000, v158
	s_nop 1
	v_addc_co_u32_e32 v9, vcc, 0, v159, vcc
	global_load_dwordx4 v[38:41], v[6:7], off
	global_load_dwordx4 v[34:37], v[8:9], off

.LBB1_232:
	s_or_b64 exec, exec, s[34:35]
	s_setprio 0
	s_movk_i32 s0, 0x200
	s_lshl_b32 s8, s10, 6
	v_cmp_gt_u32_e32 vcc, s0, v0
	s_and_saveexec_b64 s[0:1], vcc
	s_xor_b64 s[0:1], exec, s[0:1]
	s_cbranch_execnz .LBB1_235
	s_andn2_saveexec_b64 s[0:1], s[0:1]
	s_cbranch_execnz .LBB1_248
